# also the v_pk_mul_f32 of the attention accumulator-rescale blocks (FoX, SWA, cross) rewritten as scalar multiplies
# baseline (speedup 1.0000x reference)
; #define LAS __attribute__((address_space(3)))
; #define LDS_WAIT() asm volatile("s_waitcnt lgkmcnt(0)" ::: "memory")
; template <int D, bool MASK, bool BIAS, bool SINK, bool REV, bool O8, class BG>
; __device__ __forceinline__ void attn_unit(const Prm& P, LAS unsigned char* lds, BG& bg) {
;     ...
;             if (first || __any(rm > THR)) {
;                 float dl = first ? rm : __builtin_fmaxf(rm, 0.f);
;                 if (!(dl > -1e30f)) dl = 0.f;
;                 mhat += dl;
; #pragma unroll
;                 for (int r = 0; r < 16; ++r) { p0[r] -= dl; p1[r] -= dl; }
;                 if (!first) {
;                     const float f = __builtin_amdgcn_exp2f(-dl); l_reg *= f;
;                     if (hi == 0) wsf[r32] = f;
;                     LDS_WAIT();
; #pragma unroll
;                     for (int g = 0; g < 4; ++g) { const f32x4 fv = *(const LAS f32x4*)(wsf + 8 * g + 4 * hi);
; #pragma unroll
;                         for (int d = 0; d < NDB; ++d)
; #pragma unroll
;                             for (int j = 0; j < 4; ++j) o[d][4 * g + j] *= fv[j]; }
;                 }
.LBB0_471:
	s_andn2_b64 vcc, exec, s[94:95]
	s_cbranch_vccnz .LBB0_477
	v_max_f32_e32 v67, v66, v66
	v_max_f32_e32 v67, 0, v67
	v_cndmask_b32_e64 v66, v67, v66, s[92:93]
	s_and_b64 vcc, exec, s[6:7]
	s_mov_b32 s6, 0xf149f2ca
	v_cmp_lt_f32_e64 s[6:7], s6, v66
	s_nop 1
	v_cndmask_b32_e64 v66, 0, v66, s[6:7]
	s_cbranch_vccnz .LBB0_476
	v_exp_f32_e64 v67, -v66
	s_and_saveexec_b64 s[6:7], s[26:27]
	ds_write_b32 v222, v67
	s_or_b64 exec, exec, s[6:7]
	s_waitcnt lgkmcnt(0)
	ds_read_b128 v[68:71], v224
	ds_read_b128 v[72:75], v224 offset:32
	ds_read_b128 v[76:79], v224 offset:64
	ds_read_b128 v[80:83], v224 offset:96
	v_mul_f32_e32 v225, v225, v67
	s_waitcnt lgkmcnt(0)
	v_mul_f32_e32 v23, v23, v71
	v_mul_f32_e32 v22, v22, v70
	v_mul_f32_e32 v27, v27, v75
	v_mul_f32_e32 v26, v26, v74
	v_mul_f32_e32 v31, v31, v79
	v_mul_f32_e32 v30, v30, v78
	v_mul_f32_e32 v35, v35, v83
	v_mul_f32_e32 v34, v34, v82
	v_mul_f32_e32 v19, v19, v83
	v_mul_f32_e32 v18, v18, v82
	v_mul_f32_e32 v15, v15, v79
	v_mul_f32_e32 v14, v14, v78
	v_mul_f32_e32 v11, v11, v75
	v_mul_f32_e32 v10, v10, v74
	v_mul_f32_e32 v7, v7, v71
	v_mul_f32_e32 v6, v6, v70
	v_mul_f32_e32 v33, v33, v81
	v_mul_f32_e32 v32, v32, v80
	v_mul_f32_e32 v29, v29, v77
	v_mul_f32_e32 v28, v28, v76
	v_mul_f32_e32 v25, v25, v73
	v_mul_f32_e32 v24, v24, v72
	v_mul_f32_e32 v21, v21, v69
	v_mul_f32_e32 v20, v20, v68
	v_mul_f32_e32 v17, v17, v81
	v_mul_f32_e32 v16, v16, v80
	v_mul_f32_e32 v13, v13, v77
	v_mul_f32_e32 v12, v12, v76
	v_mul_f32_e32 v9, v9, v73
	v_mul_f32_e32 v8, v8, v72
	v_mul_f32_e32 v5, v5, v69
	v_mul_f32_e32 v4, v4, v68

; #define LAS __attribute__((address_space(3)))
; #define LDS_WAIT() asm volatile("s_waitcnt lgkmcnt(0)" ::: "memory")
; __device__ __forceinline__ float max3f(float a, float b, float c) { return __builtin_fmaxf(__builtin_fmaxf(a, b), c); }
; template <int D, bool MASK, bool BIAS, bool SINK, bool REV, bool O8, class BG>
; __device__ __forceinline__ void attn_unit(const Prm& P, LAS unsigned char* lds, BG& bg) {
;     ...
;             float a = max3f(p0[0], p0[1], p1[0]), b = max3f(p0[2], p0[3], p1[1]); a = max3f(a, p1[2], p1[3]);
; #pragma unroll
;             for (int r = 4; r < 16; r += 4) { a = max3f(a, p0[r], p0[r + 1]); b = max3f(b, p0[r + 2], p0[r + 3]); a = max3f(a, p1[r], p1[r + 1]); b = max3f(b, p1[r + 2], p1[r + 3]); }
;             float rm = __builtin_fmaxf(a, b);
;             { auto rr = __builtin_amdgcn_permlane32_swap(__float_as_uint(rm), __float_as_uint(rm), false, false); rm = __builtin_fmaxf(__uint_as_float(rr[0]), __uint_as_float(rr[1])); }
;             if (first || __any(rm > THR)) {
;                 float dl = first ? rm : __builtin_fmaxf(rm, 0.f);
;                 if (!(dl > -1e30f)) dl = 0.f;
;                 mhat += dl;
; #pragma unroll
;                 for (int r = 0; r < 16; ++r) { p0[r] -= dl; p1[r] -= dl; }
;                 if (!first) {
;                     const float f = __builtin_amdgcn_exp2f(-dl); l_reg *= f;
;                     if (hi == 0) wsf[r32] = f;
;                     LDS_WAIT();
; #pragma unroll
;                     for (int g = 0; g < 4; ++g) { const f32x4 fv = *(const LAS f32x4*)(wsf + 8 * g + 4 * hi);
; #pragma unroll
;                         for (int d = 0; d < NDB; ++d)
; #pragma unroll
;                             for (int j = 0; j < 4; ++j) o[d][4 * g + j] *= fv[j]; }
;                 }
.LBB0_606:
	v_max_f32_e32 v82, v51, v51
	v_max_f32_e32 v91, v50, v50
	v_max_f32_e32 v82, v91, v82
	v_max3_f32 v91, v52, v53, v35
	v_max3_f32 v82, v82, v34, v36
	v_max3_f32 v82, v82, v37, v54
	v_max3_f32 v91, v91, v56, v57
	v_max3_f32 v82, v82, v55, v38
	v_max3_f32 v91, v91, v40, v41
	v_max3_f32 v82, v82, v39, v58
	v_max3_f32 v91, v91, v60, v61
	v_max3_f32 v82, v82, v59, v42
	v_max3_f32 v91, v91, v44, v45
	v_max3_f32 v82, v82, v43, v62
	v_max3_f32 v91, v91, v64, v65
	v_max3_f32 v82, v82, v63, v46
	v_max3_f32 v91, v91, v48, v49
	v_max3_f32 v82, v82, v47, v91
	v_mov_b32_e32 v91, v82
	s_nop 1
	v_permlane32_swap_b32_e32 v82, v91
	v_max_f32_e32 v91, v91, v91
	v_max_f32_e32 v82, v82, v82
	v_max_f32_e32 v82, v82, v91
	s_mov_b32 s6, 0x41000000
	v_cmp_lt_f32_e32 vcc, s6, v82
	s_cbranch_vccz .LBB0_610
	v_max_f32_e32 v82, v82, v82
	v_max_f32_e32 v82, 0, v82
	v_exp_f32_e64 v91, -v82
	s_and_saveexec_b64 s[6:7], s[4:5]
	ds_write_b32 v189, v91
	s_or_b64 exec, exec, s[6:7]
	s_waitcnt lgkmcnt(0)
	ds_read_b128 v[192:195], v191
	ds_read_b128 v[196:199], v191 offset:32
	ds_read_b128 v[200:203], v191 offset:64
	ds_read_b128 v[204:207], v191 offset:96
	v_sub_f32_e32 v51, v51, v82
	v_sub_f32_e32 v50, v50, v82
	v_sub_f32_e32 v35, v35, v82
	v_sub_f32_e32 v34, v34, v82
	v_sub_f32_e32 v53, v53, v82
	v_sub_f32_e32 v52, v52, v82
	v_sub_f32_e32 v37, v37, v82
	v_sub_f32_e32 v36, v36, v82
	v_sub_f32_e32 v55, v55, v82
	v_sub_f32_e32 v54, v54, v82
	v_sub_f32_e32 v39, v39, v82
	v_sub_f32_e32 v38, v38, v82
	v_sub_f32_e32 v57, v57, v82
	v_sub_f32_e32 v56, v56, v82
	v_sub_f32_e32 v41, v41, v82
	v_sub_f32_e32 v40, v40, v82
	v_sub_f32_e32 v59, v59, v82
	v_sub_f32_e32 v58, v58, v82
	v_sub_f32_e32 v43, v43, v82
	v_sub_f32_e32 v42, v42, v82
	v_sub_f32_e32 v61, v61, v82
	v_sub_f32_e32 v60, v60, v82
	v_sub_f32_e32 v45, v45, v82
	v_sub_f32_e32 v44, v44, v82
	v_sub_f32_e32 v63, v63, v82
	v_sub_f32_e32 v62, v62, v82
	v_sub_f32_e32 v47, v47, v82
	v_sub_f32_e32 v46, v46, v82
	v_sub_f32_e32 v65, v65, v82
	v_sub_f32_e32 v64, v64, v82
	v_sub_f32_e32 v49, v49, v82
	v_sub_f32_e32 v48, v48, v82
	v_add_f32_e32 v188, v188, v82
	v_mul_f32_e32 v87, v87, v91
	s_waitcnt lgkmcnt(0)
	v_mul_f32_e32 v33, v33, v207
	v_mul_f32_e32 v32, v32, v206
	v_mul_f32_e32 v29, v29, v203
	v_mul_f32_e32 v28, v28, v202
	v_mul_f32_e32 v25, v25, v199
	v_mul_f32_e32 v24, v24, v198
	v_mul_f32_e32 v21, v21, v195
	v_mul_f32_e32 v20, v20, v194
	v_mul_f32_e32 v17, v17, v207
	v_mul_f32_e32 v16, v16, v206
	v_mul_f32_e32 v13, v13, v203
	v_mul_f32_e32 v12, v12, v202
	v_mul_f32_e32 v9, v9, v199
	v_mul_f32_e32 v8, v8, v198
	v_mul_f32_e32 v5, v5, v195
	v_mul_f32_e32 v4, v4, v194
	v_mul_f32_e32 v31, v31, v205
	v_mul_f32_e32 v30, v30, v204
	v_mul_f32_e32 v27, v27, v201
	v_mul_f32_e32 v26, v26, v200
	v_mul_f32_e32 v23, v23, v197
	v_mul_f32_e32 v22, v22, v196
	v_mul_f32_e32 v19, v19, v193
	v_mul_f32_e32 v18, v18, v192
	v_mul_f32_e32 v15, v15, v205
	v_mul_f32_e32 v14, v14, v204
	v_mul_f32_e32 v11, v11, v201
	v_mul_f32_e32 v10, v10, v200
	v_mul_f32_e32 v7, v7, v197
	v_mul_f32_e32 v6, v6, v196
	v_mul_f32_e32 v3, v3, v193
	v_mul_f32_e32 v2, v2, v192

; #define LAS __attribute__((address_space(3)))
; #define LDS_WAIT() asm volatile("s_waitcnt lgkmcnt(0)" ::: "memory")
; template <int D, bool MASK, bool BIAS, bool SINK, bool REV, bool O8, class BG>
; __device__ __forceinline__ void attn_unit(const Prm& P, LAS unsigned char* lds, BG& bg) {
;     ...
;                 if (!first) {
;                     const float f = __builtin_amdgcn_exp2f(-dl); l_reg *= f;
;                     if (hi == 0) wsf[r32] = f;
;                     LDS_WAIT();
; #pragma unroll
;                     for (int g = 0; g < 4; ++g) { const f32x4 fv = *(const LAS f32x4*)(wsf + 8 * g + 4 * hi);
; #pragma unroll
;                         for (int d = 0; d < NDB; ++d)
; #pragma unroll
;                             for (int j = 0; j < 4; ++j) o[d][4 * g + j] *= fv[j]; }
;                 }
.LBB0_938:
	s_or_b64 exec, exec, s[4:5]
	s_waitcnt lgkmcnt(0)
	v_add_u32_e32 v151, s72, v143
	ds_read_b128 v[152:155], v151 offset:96
	ds_read_b128 v[156:159], v151 offset:64
	ds_read_b128 v[160:163], v151 offset:32
	ds_read_b128 v[164:167], v151
	v_mul_f32_e32 v149, v149, v135
	s_waitcnt lgkmcnt(0)
	v_mul_f32_e32 v65, v65, v153
	v_mul_f32_e32 v64, v64, v152
	v_mul_f32_e32 v61, v61, v157
	v_mul_f32_e32 v60, v60, v156
	v_mul_f32_e32 v57, v57, v161
	v_mul_f32_e32 v56, v56, v160
	v_mul_f32_e32 v67, v67, v155
	v_mul_f32_e32 v66, v66, v154
	v_mul_f32_e32 v63, v63, v159
	v_mul_f32_e32 v62, v62, v158
	v_mul_f32_e32 v59, v59, v163
	v_mul_f32_e32 v58, v58, v162
	v_mul_f32_e32 v55, v55, v167
	v_mul_f32_e32 v54, v54, v166
	v_mul_f32_e32 v53, v53, v165
	v_mul_f32_e32 v52, v52, v164
	v_mul_f32_e32 v49, v49, v153
	v_mul_f32_e32 v48, v48, v152
	v_mul_f32_e32 v45, v45, v157
	v_mul_f32_e32 v44, v44, v156
	v_mul_f32_e32 v41, v41, v161
	v_mul_f32_e32 v40, v40, v160
	v_mul_f32_e32 v51, v51, v155
	v_mul_f32_e32 v50, v50, v154
	v_mul_f32_e32 v47, v47, v159
	v_mul_f32_e32 v46, v46, v158
	v_mul_f32_e32 v43, v43, v163
	v_mul_f32_e32 v42, v42, v162
	v_mul_f32_e32 v39, v39, v167
	v_mul_f32_e32 v38, v38, v166
	v_mul_f32_e32 v37, v37, v165
	v_mul_f32_e32 v36, v36, v164
	v_mul_f32_e32 v33, v33, v153
	v_mul_f32_e32 v32, v32, v152
	v_mul_f32_e32 v29, v29, v157
	v_mul_f32_e32 v28, v28, v156
	v_mul_f32_e32 v25, v25, v161
	v_mul_f32_e32 v24, v24, v160
	v_mul_f32_e32 v35, v35, v155
	v_mul_f32_e32 v34, v34, v154
	v_mul_f32_e32 v31, v31, v159
	v_mul_f32_e32 v30, v30, v158
	v_mul_f32_e32 v27, v27, v163
	v_mul_f32_e32 v26, v26, v162
	v_mul_f32_e32 v23, v23, v167
	v_mul_f32_e32 v22, v22, v166
	v_mul_f32_e32 v21, v21, v165
	v_mul_f32_e32 v20, v20, v164
	v_mul_f32_e32 v17, v17, v153
	v_mul_f32_e32 v16, v16, v152
	v_mul_f32_e32 v13, v13, v157
	v_mul_f32_e32 v12, v12, v156
	v_mul_f32_e32 v9, v9, v161
	v_mul_f32_e32 v8, v8, v160
	v_mul_f32_e32 v19, v19, v155
	v_mul_f32_e32 v18, v18, v154
	v_mul_f32_e32 v15, v15, v159
	v_mul_f32_e32 v14, v14, v158
	v_mul_f32_e32 v11, v11, v163
	v_mul_f32_e32 v10, v10, v162
	v_mul_f32_e32 v7, v7, v167
	v_mul_f32_e32 v6, v6, v166
	v_mul_f32_e32 v5, v5, v165
	v_mul_f32_e32 v4, v4, v164
